# part D conversion in FFN1 epilogues (dwordx4 loads) + grid-size guard: any grid other than 256 workgroups keeps the conversion in norm1 as the baseline does
# speedup vs baseline: 1.0081x; 1.0033x over previous
.LBB0_254:
	s_or_b64 exec, exec, s[26:27]
	v_readlane_b32 s0, v254, 10
	s_cmp_lg_u32 s0, 0
	s_cselect_b64 s[26:27], -1, 0
	s_cmp_lg_u32 s0, 3
	s_cselect_b64 s[36:37], -1, 0
	s_waitcnt lgkmcnt(0)
	s_add_u32 s6, s10, 0x1bb0000
	s_addc_u32 s21, s11, 0
	s_add_u32 s25, s10, 0x9bb0000
	v_cmp_ne_u32_e64 s[38:39], 2, v2
	s_mov_b32 s3, 0
	v_lshlrev_b64 v[28:29], 27, v[4:5]
	s_addc_u32 s35, s11, 0
	s_lshl_b32 s58, s12, 2
	s_lshl_b32 s59, s12, 1
	s_lshl_b32 s60, s12, 7
	s_lshl_b32 s61, s12, 8
	s_lshl_b32 s62, s12, 6
	s_cmpk_lg_u32 s12, 0x100
	s_cselect_b32 s32, 4, 3
	v_readlane_b32 s1, v254, 11
	s_branch .LBB0_256
.LBB0_255:
	s_or_b64 exec, exec, s[10:11]
	s_add_i32 s3, s3, 1
	s_cmp_lg_u32 s3, s32
	s_cbranch_scc0 .LBB0_324

.LBB0_1908:
	v_readlane_b32 s78, v254, 2
	v_readlane_b32 s79, v254, 3
	v_readlane_b32 s72, v254, 10
	v_lshrrev_b32_e32 v2, 6, v0
	s_nop 4
	s_load_dwordx2 s[80:81], s[78:79], 0x100
	s_load_dwordx2 s[78:79], s[78:79], 0x118
	v_readfirstlane_b32 s32, v2
	s_waitcnt lgkmcnt(0)
	s_lshl_b32 s72, s72, 27
	s_add_u32 s80, s80, s72
	s_addc_u32 s81, s81, 0
	s_and_b32 s72, s32, 1
	s_lshl_b32 s72, s72, 17
	s_add_u32 s80, s80, s72
	s_addc_u32 s81, s81, 0
	s_add_u32 s78, s78, 0x9bb0000
	s_addc_u32 s79, s79, 0
	s_and_b32 s72, s32, 1
	s_lshl_b32 s72, s72, 5
	s_add_u32 s78, s78, s72
	s_addc_u32 s79, s79, 0
	s_lshr_b32 s72, s32, 1
	s_lshl_b32 s72, s72, 8
	s_load_dword s32, s[96:97], 0x0
	s_waitcnt lgkmcnt(0)
	s_cmpk_lg_u32 s32, 0x100
	s_cselect_b32 s72, 0x7fff0000, s72
	v_writelane_b32 v255, s80, 40
	v_writelane_b32 v255, s81, 41
	v_writelane_b32 v255, s78, 42
	v_writelane_b32 v255, s79, 43
	v_writelane_b32 v255, s72, 44
	s_mov_b32 s32, 0
	v_readlane_b32 s8, v255, 3
	v_readlane_b32 s9, v255, 4
	s_and_b64 s[8:9], s[8:9], exec
	v_readlane_b32 s0, v254, 2
	s_cselect_b32 s3, 16, 17
	v_readlane_b32 s1, v254, 3
	v_mov_b32_e32 v2, v0
	s_lshl_b32 s8, s3, 8
	s_mov_b32 s6, s2
	s_cmp_ge_i32 s6, s8
	v_readfirstlane_b32 s10, v2
	s_cbranch_scc1 .LBB0_1922
	s_waitcnt vmcnt(0)
	v_ashrrev_i32_e32 v5, 31, v2
	v_lshrrev_b32_e32 v5, 26, v5
	v_add_u32_e32 v5, v2, v5
	v_ashrrev_i32_e32 v12, 6, v5
	v_bfe_i32 v5, v2, 27, 1
	v_lshlrev_b32_e32 v4, 4, v2
	v_lshrrev_b32_e32 v5, 22, v5
	v_add_u32_e32 v5, v4, v5
	v_and_b32_e32 v5, 0xfffffc00, v5
	v_sub_u32_e32 v5, v4, v5
	v_lshrrev_b32_e32 v6, 4, v5
	s_load_dwordx2 s[38:39], s[0:1], 0x118
	v_bitop3_b32 v13, v6, v5, 32 bitop3:0x6c
	v_ashrrev_i32_e32 v5, 31, v5
	v_lshrrev_b32_e32 v5, 26, v5
	v_add_u32_e32 v5, v13, v5
	v_add_u32_e32 v4, 0x2000, v4
	v_ashrrev_i32_e32 v14, 6, v5
	v_ashrrev_i32_e32 v5, 31, v4
	v_lshrrev_b32_e32 v5, 22, v5
	s_waitcnt lgkmcnt(0)
	s_add_u32 s26, s38, 0x163b0000
	v_add_u32_e32 v5, v4, v5
	s_addc_u32 s27, s39, 0
	v_ashrrev_i32_e32 v15, 10, v5
	s_add_u32 s11, s38, 0x1bb0000
	v_mul_i32_i24_e32 v5, 0x400, v15
	s_addc_u32 s12, s39, 0
	v_sub_u32_e32 v4, v4, v5
	s_add_u32 s21, s38, 0x233f0000
	v_lshrrev_b32_e32 v5, 4, v4
	s_addc_u32 s25, s39, 0
	v_bitop3_b32 v16, v5, v4, 32 bitop3:0x6c
	v_lshlrev_b32_e32 v5, 3, v12
	s_lshl_b32 s59, s3, 4
	v_and_b32_e32 v5, -16, v5
	s_abs_i32 s60, s59
	v_add_u32_e32 v6, v14, v5
	v_cvt_f32_u32_e32 v5, s60
	s_ashr_i32 s9, s6, 31
	s_lshr_b32 s9, s9, 29
	s_add_i32 s9, s6, s9
	v_rcp_iflag_f32_e32 v5, v5
	s_ashr_i32 s36, s9, 3
	s_and_b32 s9, s9, -8
	s_sub_i32 s6, s6, s9
	v_mul_f32_e32 v5, 0x4f7ffffe, v5
	v_cvt_u32_f32_e32 v5, v5
	s_lshl_b32 s58, s3, 5
	s_lshr_b32 s9, s6, 31
	s_or_b32 s9, s9, s58
	s_mul_i32 s6, s9, s6
	s_add_i32 s6, s6, s36
	s_sub_i32 s36, 0, s60
	v_readfirstlane_b32 s62, v5
	s_mul_i32 s36, s36, s62
	s_ashr_i32 s9, s6, 31
	s_bfe_i32 s61, s3, 0x1001b
	s_mul_hi_u32 s36, s62, s36
	s_xor_b32 s3, s9, s61
	s_abs_i32 s9, s6
	s_add_i32 s62, s62, s36
	s_mul_hi_u32 s36, s9, s62
	s_mul_i32 s37, s36, s60
	s_ashr_i32 s1, s10, 6
	s_sub_i32 s9, s9, s37
	s_ashr_i32 s0, s10, 8
	s_lshl_b32 s56, s1, 10
	s_add_i32 s37, s36, 1
	s_sub_i32 s40, s9, s60
	s_cmp_ge_u32 s9, s60
	s_cselect_b32 s36, s37, s36
	s_cselect_b32 s9, s40, s9
	s_add_i32 s37, s36, 1
	s_cmp_ge_u32 s9, s60
	s_cselect_b32 s9, s37, s36
	s_xor_b32 s9, s9, s3
	s_sub_i32 s40, s9, s3
	s_mul_i32 s3, s40, s59
	s_sub_i32 s3, s6, s3
	s_bfe_u32 s9, s3, 0x4001b
	s_add_i32 s9, s3, s9
	s_sext_i32_i16 s36, s9
	v_ashrrev_i32_e32 v4, 31, v16
	s_mul_i32 s6, s40, 17
	s_ashr_i32 s36, s36, 4
	v_lshrrev_b32_e32 v4, 26, v4
	s_add_i32 s48, s6, s36
	v_add_u32_e32 v17, v16, v4
	v_lshlrev_b32_e32 v4, 3, v15
	s_and_b32 s6, s9, 0xfff0
	s_ashr_i32 s49, s48, 31
	v_ashrrev_i32_e32 v18, 6, v17
	v_and_b32_e32 v4, -16, v4
	s_sub_i32 s42, s3, s6
	s_lshl_b64 s[36:37], s[48:49], 10
	v_add_u32_e32 v4, v18, v4
	s_add_u32 s36, s21, s36
	s_addc_u32 s37, s25, s37
	v_ashrrev_i32_e32 v7, 31, v6
	v_ashrrev_i32_e32 v5, 31, v4
	v_mov_b32_e32 v117, 0x7a7a7a7a
	v_mov_b32_e32 v198, 0x7f7f7f7f
	v_lshl_add_u64 v[8:9], v[6:7], 2, s[36:37]
	v_lshl_add_u64 v[10:11], v[4:5], 2, s[36:37]
	s_load_dword s57, s[96:97], 0x0
	global_load_dword v19, v[8:9], off
	global_load_dword v20, v[10:11], off
	s_nop 0
	global_load_dword v10, v[10:11], off offset:512
	s_nop 0
	global_load_dword v8, v[8:9], off offset:512
	v_mul_i32_i24_e32 v11, 64, v14
	v_sub_u32_e32 v11, v13, v11
	v_lshlrev_b32_e32 v9, 5, v12
	v_ashrrev_i16_sdwa v11, v250, sext(v11) dst_sel:DWORD dst_unused:UNUSED_PAD src0_sel:DWORD src1_sel:BYTE_0
	v_and_b32_e32 v9, 32, v9
	v_bfe_i32 v11, v11, 0, 16
	v_add_lshl_u32 v199, v9, v11, 1
	v_and_b32_e32 v11, 0xc0, v17
	v_sub_u32_e32 v11, v16, v11
	v_lshlrev_b32_e32 v9, 5, v15
	v_ashrrev_i16_sdwa v11, v250, sext(v11) dst_sel:DWORD dst_unused:UNUSED_PAD src0_sel:DWORD src1_sel:BYTE_0
	v_and_b32_e32 v9, 32, v9
	v_bfe_i32 v11, v11, 0, 16
	v_add_lshl_u32 v200, v9, v11, 1
	v_and_b32_e32 v9, 3, v18
	s_mov_b32 s3, 0x3fffe0
	v_lshrrev_b32_e32 v11, 2, v4
	v_lshlrev_b32_e32 v12, 1, v4
	v_and_or_b32 v9, v4, s3, v9
	v_and_b32_e32 v11, 4, v11
	v_and_b32_e32 v12, 24, v12
	v_or3_b32 v9, v9, v11, v12
	s_ashr_i32 s41, s40, 31
	v_lshl_add_u32 v166, v9, 10, v200
	v_and_b32_e32 v9, 3, v14
	s_lshl_b64 s[40:41], s[40:41], 22
	v_and_or_b32 v9, v6, s3, v9
	s_add_u32 s3, s11, s40
	s_addc_u32 s6, s12, s41
	s_bfe_i64 s[40:41], s[42:43], 0x100000
	v_lshrrev_b32_e32 v11, 2, v6
	v_lshlrev_b32_e32 v12, 1, v6
	s_lshl_b64 s[40:41], s[40:41], 18
	v_and_b32_e32 v11, 4, v11
	v_and_b32_e32 v12, 24, v12
	s_add_u32 s50, s3, s40
	v_or3_b32 v9, v9, v11, v12
	s_addc_u32 s51, s6, s41
	s_add_i32 s49, s56, 0
	v_lshl_add_u32 v168, v9, 10, v199
	s_add_i32 m0, s49, 0x10400
	s_add_i32 s63, s49, 0x400
	global_load_lds_dwordx4 v168, s[50:51]
	s_add_i32 m0, s49, 0x12400
	s_add_i32 s64, s49, 0x2400
	global_load_lds_dwordx4 v166, s[50:51]
	s_mov_b32 m0, s63
	s_add_u32 s40, s50, 0x20000
	s_addc_u32 s41, s51, 0
	s_add_i32 s65, s49, 0x4400
	s_add_i32 s66, s49, 0x6400
	v_mov_b32_e32 v169, v3
	v_mov_b32_e32 v167, v3
	v_mov_b32_e32 v185, v3
	v_mov_b32_e32 v181, v3
	v_lshl_add_u64 v[14:15], s[50:51], 0, v[168:169]
	v_lshl_add_u64 v[12:13], s[50:51], 0, v[166:167]
	s_waitcnt vmcnt(0)
	v_lshl_add_u32 v184, v19, 10, v199
	v_lshl_add_u32 v180, v20, 10, v200
	global_load_lds_dwordx4 v184, s[26:27]
	s_mov_b32 m0, s64
	v_lshl_add_u32 v178, v8, 10, v199
	global_load_lds_dwordx4 v180, s[26:27]
	s_add_i32 m0, s49, 0x14400
	v_lshl_add_u32 v176, v10, 10, v200
	global_load_lds_dwordx4 v168, s[40:41]
	s_add_i32 m0, s49, 0x16400
	v_lshl_add_u64 v[10:11], s[26:27], 0, v[184:185]
	global_load_lds_dwordx4 v166, s[40:41]
	s_mov_b32 m0, s65
	s_cmp_lg_u32 s0, 1
	global_load_lds_dwordx4 v178, s[26:27]
	s_mov_b32 m0, s66
	v_lshl_add_u64 v[8:9], s[26:27], 0, v[180:181]
	global_load_lds_dwordx4 v176, s[26:27]
	s_cbranch_scc1 .LBB0_1911
	s_barrier
